# GEMM phase prologues (6): K-tile 1 stage loads requested before waiting for K-tile 0 (one exposed latency per phase start instead of two), on top of chain DMA reorder
# speedup vs baseline: 1.0053x; 1.0007x over previous
; #define PG8_STAGE(bufoff, gbase, voff) do { _Pragma("unroll") for (int _i = 0; _i < 2; ++_i) \
;         __builtin_amdgcn_global_load_lds((const unsigned*)((const char*)(gbase) + (voff)[_i]), (LAS unsigned*)(lds + (bufoff) + ldsw + _i * 8192), 16, 0, 0); } while (0)
; #define PG8_WAIT_V(n) asm volatile("s_waitcnt vmcnt(" #n ")" ::: "memory")
; #define PG8_BAR __builtin_amdgcn_s_barrier()
; template <class Epi, class Sched, bool F8 = false>
; DI void gemm_phase(LAS unsigned char* lds, const int K, const Sched& S, const Epi& E) {
;     ...
;     unsigned oA[2][2]; S.a_off(cur, tid, oA);
;     const char* cA = S.a_base(cur); const char* cB = S.b_base(cur);
;     PG8_STAGE(PG8_SB(0, 0), cB, voffB); PG8_STAGE(PG8_SB(0, 1), cB + hstep, voffB); PG8_STAGE(PG8_SA(0, 0), cA, oA[0]); PG8_STAGE(PG8_SA(0, 1), cA, oA[1]);
;     if (wr == 1) PG8_BAR;
;     PG8_WAIT_V(2); PG8_BAR;
;     PG8_STAGE(PG8_SB(1, 0), cB + kstep, voffB); PG8_STAGE(PG8_SA(1, 0), cA + kstep, oA[0]); PG8_STAGE(PG8_SB(1, 1), cB + hstep + kstep, voffB);
;     PG8_WAIT_V(6); PG8_BAR;
.LBB0_270:
	s_add_u32 s6, s58, 0x20bc0000
	s_addc_u32 s7, s59, 0
	v_writelane_b32 v255, s6, 16
	v_lshl_add_u64 v[12:13], v[12:13], 0, s[24:25]
	v_writelane_b32 v255, s7, 17
	s_add_u32 s6, s58, 0x22bc0000
	s_addc_u32 s7, s59, 0
	v_writelane_b32 v255, s6, 18
	v_lshl_add_u64 v[10:11], v[10:11], 0, s[24:25]
	v_lshl_add_u64 v[6:7], v[6:7], 0, s[24:25]
	v_writelane_b32 v255, s7, 19
	s_add_u32 s6, s58, 0x24bc0000
	s_addc_u32 s7, s59, 0
	v_writelane_b32 v255, s6, 20
	v_bfe_u32 v5, v14, 4, 2
	v_and_b32_e32 v1, 15, v14
	v_writelane_b32 v255, s7, 21
	s_add_u32 s6, s58, 0x28bc0000
	s_addc_u32 s7, s59, 0
	v_writelane_b32 v255, s6, 22
	s_mov_b32 s11, s69
	v_mov_b32_e32 v171, v4
	v_writelane_b32 v255, s7, 23
	s_add_u32 s6, s58, 0x3ebc0000
	s_addc_u32 s7, s59, 0
	v_writelane_b32 v255, s6, 24
	v_mov_b32_e32 v175, v4
	s_mov_b32 s96, 0
	v_writelane_b32 v255, s7, 25
	s_add_u32 s6, s58, 0x209c0000
	s_addc_u32 s7, s59, 0
	v_writelane_b32 v255, s6, 26
	s_nop 1
	v_writelane_b32 v255, s7, 27
	v_readlane_b32 s6, v254, 62
	v_readlane_b32 s7, v254, 63
	s_lshl_b64 s[6:7], s[6:7], 2
	s_add_u32 s74, s40, s6
	v_writelane_b32 v255, s40, 28
	s_addc_u32 s75, s41, s7
	s_add_i32 s88, s68, 0x18000
	s_and_b32 s5, s4, 3
	s_add_i32 s89, s88, s0
	s_lshl_b32 s87, s1, 6
	s_lshl_b32 s1, s1, 13
	s_lshl_b32 s10, s5, 5
	s_lshl_b32 s8, s5, 12
	s_mov_b32 m0, s89
	s_add_i32 s90, s89, 0x2000
	s_add_i32 s91, s83, 0x8000
	s_add_i32 s92, s83, 0xa000
	global_load_lds_dwordx4 v[12:13], off
	s_mov_b32 m0, s90
	s_add_u32 s6, s66, 0x20080
	global_load_lds_dwordx4 v[10:11], off
	s_mov_b32 m0, s91
	s_addc_u32 s7, s67, 0
	s_add_i32 s93, s68, 0x1c000
	global_load_lds_dwordx4 v[6:7], off
	v_lshl_add_u64 v[6:7], v[8:9], 0, s[24:25]
	s_mov_b32 m0, s92
	s_add_i32 s94, s93, s0
	global_load_lds_dwordx4 v[6:7], off
	v_lshl_add_u64 v[6:7], s[6:7], 0, v[2:3]
	s_mov_b32 m0, s94
	s_add_i32 s95, s94, 0x2000
	global_load_lds_dwordx4 v[6:7], off
	v_lshl_add_u64 v[6:7], s[6:7], 0, v[166:167]
	s_mov_b32 m0, s95
	v_writelane_b32 v255, s41, 29
	global_load_lds_dwordx4 v[6:7], off
	v_lshlrev_b32_e32 v6, 4, v5
	v_lshlrev_b32_e32 v7, 2, v14
	v_lshl_or_b32 v6, v1, 6, v6
	v_and_b32_e32 v7, 32, v7
	v_bitop3_b32 v8, v6, s1, v7 bitop3:0xde
	v_bitop3_b32 v188, v6, s8, v7 bitop3:0xde
	v_lshlrev_b32_e32 v6, 12, v19
	v_writelane_b32 v255, s42, 30
	s_cmp_lt_u32 s4, 4
	v_and_b32_e32 v6, 0x7fffe000, v6
	v_writelane_b32 v255, s43, 31
	s_cselect_b64 s[0:1], -1, 0
	s_bfe_u32 s2, s4, 0x10001
	v_lshl_add_u32 v6, v20, 9, v6
	v_writelane_b32 v255, s2, 32
	v_or_b32_e32 v6, v6, v21
	v_writelane_b32 v255, s10, 36
	s_and_b32 s4, s10, 32
	v_add_u32_sdwa v6, v6, sext(v22) dst_sel:DWORD dst_unused:UNUSED_PAD src0_sel:DWORD src1_sel:WORD_0
	v_mov_b32_e32 v9, 0x20000
	s_cmp_eq_u32 s5, 0
	v_lshl_add_u32 v6, v6, 1, v9
	v_mov_b32_e32 v7, v4
	s_cselect_b64 s[6:7], -1, 0
	s_lshl_b32 s97, s5, 15
	s_ashr_i32 s38, s49, 31
	s_ashr_i32 s39, s60, 31
	v_lshl_add_u64 v[176:177], v[6:7], 0, s[26:27]
	v_lshlrev_b32_e32 v6, 12, v15
	s_add_u32 s4, s58, s4
	v_and_b32_e32 v6, 0x7fffe000, v6
	s_addc_u32 s5, s59, 0
	v_lshl_add_u32 v6, v16, 9, v6
	s_add_u32 s4, s4, 0x38bc0000
	v_or_b32_e32 v6, v6, v17
	s_waitcnt vmcnt(8)
	s_barrier
	s_waitcnt vmcnt(6)
	v_writelane_b32 v255, s11, 37
	s_addc_u32 s5, s5, 0
	v_add_u32_sdwa v6, v6, sext(v18) dst_sel:DWORD dst_unused:UNUSED_PAD src0_sel:DWORD src1_sel:WORD_0
	v_writelane_b32 v254, s6, 34
	v_writelane_b32 v255, s4, 38
	v_lshl_add_u32 v6, v6, 1, v9
	v_writelane_b32 v254, s7, 35
	v_writelane_b32 v255, s5, 39
	v_lshl_add_u64 v[178:179], v[6:7], 0, s[26:27]
	v_add_u32_e32 v189, s68, v8
	s_movk_i32 s2, 0x271
	s_barrier
	s_branch .LBB0_273

; #define PG8_STAGE(bufoff, gbase, voff) do { _Pragma("unroll") for (int _i = 0; _i < 2; ++_i) \
;         __builtin_amdgcn_global_load_lds((const unsigned*)((const char*)(gbase) + (voff)[_i]), (LAS unsigned*)(lds + (bufoff) + ldsw + _i * 8192), 16, 0, 0); } while (0)
; #define PG8_WAIT_V(n) asm volatile("s_waitcnt vmcnt(" #n ")" ::: "memory")
; #define PG8_BAR __builtin_amdgcn_s_barrier()
; template <class Epi, class Sched, bool F8 = false>
; DI void gemm_phase(LAS unsigned char* lds, const int K, const Sched& S, const Epi& E) {
;     ...
;     unsigned oA[2][2]; S.a_off(cur, tid, oA);
;     const char* cA = S.a_base(cur); const char* cB = S.b_base(cur);
;     PG8_STAGE(PG8_SB(0, 0), cB, voffB); PG8_STAGE(PG8_SB(0, 1), cB + hstep, voffB); PG8_STAGE(PG8_SA(0, 0), cA, oA[0]); PG8_STAGE(PG8_SA(0, 1), cA, oA[1]);
;     if (wr == 1) PG8_BAR;
;     PG8_WAIT_V(2); PG8_BAR;
;     PG8_STAGE(PG8_SB(1, 0), cB + kstep, voffB); PG8_STAGE(PG8_SA(1, 0), cA + kstep, oA[0]); PG8_STAGE(PG8_SB(1, 1), cB + hstep + kstep, voffB);
;     PG8_WAIT_V(6); PG8_BAR;
.LBB0_893:
	s_add_u32 s30, s40, 0x1c9c0000
	s_addc_u32 s31, s41, 0
	s_add_u32 s42, s40, 0x3ebc0000
	s_addc_u32 s43, s41, 0
	s_lshl_b32 s10, s8, 5
	s_add_i32 s85, s6, 0x18000
	s_and_b32 s84, s10, 0x60
	s_add_i32 s86, s85, s9
	s_lshl_b32 s83, s7, 6
	s_lshl_b32 s7, s7, 13
	s_lshl_b32 s40, s84, 7
	v_lshl_add_u64 v[12:13], v[12:13], 0, s[24:25]
	s_mov_b32 m0, s86
	s_add_i32 s87, s86, 0x2000
	s_add_i32 s88, s79, 0x8000
	s_add_i32 s89, s79, 0xa000
	global_load_lds_dwordx4 v[12:13], off
	v_lshl_add_u64 v[10:11], v[10:11], 0, s[24:25]
	s_mov_b32 m0, s87
	s_add_u32 s10, s58, 0x20080
	global_load_lds_dwordx4 v[10:11], off
	v_lshl_add_u64 v[6:7], v[6:7], 0, s[24:25]
	s_mov_b32 m0, s88
	s_addc_u32 s11, s59, 0
	s_add_i32 s90, s6, 0x1c000
	global_load_lds_dwordx4 v[6:7], off
	v_lshl_add_u64 v[6:7], v[8:9], 0, s[24:25]
	s_mov_b32 m0, s89
	s_add_i32 s91, s90, s9
	global_load_lds_dwordx4 v[6:7], off
	v_lshl_add_u64 v[6:7], s[10:11], 0, v[2:3]
	s_mov_b32 m0, s91
	s_add_i32 s92, s91, 0x2000
	global_load_lds_dwordx4 v[6:7], off
	v_lshl_add_u64 v[6:7], s[10:11], 0, v[166:167]
	s_mov_b32 m0, s92
	v_bfe_u32 v5, v14, 4, 2
	global_load_lds_dwordx4 v[6:7], off
	v_and_b32_e32 v1, 15, v14
	v_lshlrev_b32_e32 v6, 4, v5
	v_lshlrev_b32_e32 v7, 2, v14
	v_lshl_or_b32 v6, v1, 6, v6
	v_and_b32_e32 v7, 32, v7
	v_bitop3_b32 v8, v6, s7, v7 bitop3:0xde
	v_bitop3_b32 v206, v6, s40, v7 bitop3:0xde
	v_lshlrev_b32_e32 v6, 12, v19
	v_and_b32_e32 v6, 0x7fffe000, v6
	v_lshl_add_u32 v6, v20, 9, v6
	v_or_b32_e32 v6, v6, v21
	v_add_u32_sdwa v6, v6, sext(v22) dst_sel:DWORD dst_unused:UNUSED_PAD src0_sel:DWORD src1_sel:WORD_0
	v_mov_b32_e32 v9, 0x20000
	v_lshl_add_u32 v6, v6, 1, v9
	v_mov_b32_e32 v7, v4
	v_lshl_add_u64 v[176:177], v[6:7], 0, s[26:27]
	v_lshlrev_b32_e32 v6, 12, v15
	v_and_b32_e32 v6, 0x7fffe000, v6
	v_lshl_add_u32 v6, v16, 9, v6
	v_or_b32_e32 v6, v6, v17
	s_waitcnt vmcnt(8)
	s_barrier
	s_waitcnt vmcnt(6)
	v_add_u32_sdwa v6, v6, sext(v18) dst_sel:DWORD dst_unused:UNUSED_PAD src0_sel:DWORD src1_sel:WORD_0
	s_cmp_lt_u32 s8, 4
	v_lshl_add_u32 v6, v6, 1, v9
	v_mov_b32_e32 v171, v4
	v_mov_b32_e32 v175, v4
	s_sext_i32_i8 s55, s44
	s_cselect_b64 s[44:45], -1, 0
	s_ashr_i32 s93, s4, 31
	v_lshl_add_u64 v[178:179], v[6:7], 0, s[26:27]
	s_mov_b32 s94, 0
	v_add_u32_e32 v214, s6, v8
	s_barrier
	s_branch .LBB0_896

; #define PG8_STAGE(bufoff, gbase, voff) do { _Pragma("unroll") for (int _i = 0; _i < 2; ++_i) \
;         __builtin_amdgcn_global_load_lds((const unsigned*)((const char*)(gbase) + (voff)[_i]), (LAS unsigned*)(lds + (bufoff) + ldsw + _i * 8192), 16, 0, 0); } while (0)
; #define PG8_WAIT_V(n) asm volatile("s_waitcnt vmcnt(" #n ")" ::: "memory")
; #define PG8_BAR __builtin_amdgcn_s_barrier()
; template <class Epi, class Sched, bool F8 = false>
; DI void gemm_phase(LAS unsigned char* lds, const int K, const Sched& S, const Epi& E) {
;     ...
;     unsigned oA[2][2]; S.a_off(cur, tid, oA);
;     const char* cA = S.a_base(cur); const char* cB = S.b_base(cur);
;     PG8_STAGE(PG8_SB(0, 0), cB, voffB); PG8_STAGE(PG8_SB(0, 1), cB + hstep, voffB); PG8_STAGE(PG8_SA(0, 0), cA, oA[0]); PG8_STAGE(PG8_SA(0, 1), cA, oA[1]);
;     if (wr == 1) PG8_BAR;
;     PG8_WAIT_V(2); PG8_BAR;
;     PG8_STAGE(PG8_SB(1, 0), cB + kstep, voffB); PG8_STAGE(PG8_SA(1, 0), cA + kstep, oA[0]); PG8_STAGE(PG8_SB(1, 1), cB + hstep + kstep, voffB);
;     PG8_WAIT_V(6); PG8_BAR;
.LBB0_964:
	s_sext_i32_i8 s97, s30
	s_add_u32 s30, s40, 0x1c9c0000
	s_addc_u32 s31, s41, 0
	s_add_u32 s42, s40, 0x3ebc0400
	s_addc_u32 s43, s41, 0
	v_bfe_u32 v5, v14, 4, 2
	s_add_u32 s44, s40, 0x126c0000
	v_and_b32_e32 v1, 15, v14
	v_lshlrev_b32_e32 v15, 4, v5
	v_lshlrev_b32_e32 v14, 2, v14
	s_addc_u32 s45, s41, 0
	v_lshl_or_b32 v15, v1, 6, v15
	s_lshl_b32 s10, s46, 13
	v_and_b32_e32 v14, 32, v14
	v_bitop3_b32 v16, v15, s10, v14 bitop3:0xde
	s_lshl_b32 s10, s9, 5
	s_add_i32 s88, s6, 0x18000
	s_and_b32 s87, s10, 0x60
	s_add_i32 s89, s88, s47
	s_lshl_b32 s86, s46, 6
	s_lshl_b32 s10, s87, 7
	v_lshl_add_u64 v[12:13], v[12:13], 0, s[24:25]
	s_mov_b32 m0, s89
	s_add_i32 s90, s89, 0x2000
	s_add_i32 s91, s82, 0x8000
	s_add_i32 s92, s82, 0xa000
	v_bitop3_b32 v196, v15, s10, v14 bitop3:0xde
	global_load_lds_dwordx4 v[12:13], off
	v_lshl_add_u64 v[10:11], v[10:11], 0, s[24:25]
	s_mov_b32 m0, s90
	s_add_u32 s10, s66, 0x10080
	global_load_lds_dwordx4 v[10:11], off
	v_lshl_add_u64 v[6:7], v[6:7], 0, s[24:25]
	s_mov_b32 m0, s91
	s_addc_u32 s11, s67, 0
	s_add_i32 s93, s6, 0x1c000
	global_load_lds_dwordx4 v[6:7], off
	v_lshl_add_u64 v[6:7], v[8:9], 0, s[24:25]
	s_mov_b32 m0, s92
	s_add_i32 s94, s93, s47
	global_load_lds_dwordx4 v[6:7], off
	v_lshl_add_u64 v[6:7], s[10:11], 0, v[2:3]
	s_mov_b32 m0, s94
	s_add_i32 s95, s94, 0x2000
	global_load_lds_dwordx4 v[6:7], off
	v_lshl_add_u64 v[6:7], s[10:11], 0, v[134:135]
	s_mov_b32 m0, s95
	s_cmp_lt_u32 s9, 4
	global_load_lds_dwordx4 v[6:7], off
	s_waitcnt vmcnt(8)
	s_barrier
	s_waitcnt vmcnt(6)
	s_cselect_b64 s[46:47], -1, 0
	s_ashr_i32 s96, s4, 31
	s_add_u32 s48, s4, s7
	v_mov_b32_e32 v139, v4
	v_mov_b32_e32 v143, v4
	s_addc_u32 s49, s96, s8
	v_add_u32_e32 v197, s6, v16
	s_barrier
	s_branch .LBB0_967

; #define PG8_STAGE(bufoff, gbase, voff) do { _Pragma("unroll") for (int _i = 0; _i < 2; ++_i) \
;         __builtin_amdgcn_global_load_lds((const unsigned*)((const char*)(gbase) + (voff)[_i]), (LAS unsigned*)(lds + (bufoff) + ldsw + _i * 8192), 16, 0, 0); } while (0)
; #define PG8_WAIT_V(n) asm volatile("s_waitcnt vmcnt(" #n ")" ::: "memory")
; #define PG8_BAR __builtin_amdgcn_s_barrier()
; template <class Epi, class Sched, bool F8 = false>
; DI void gemm_phase(LAS unsigned char* lds, const int K, const Sched& S, const Epi& E) {
;     ...
;     unsigned oA[2][2]; S.a_off(cur, tid, oA);
;     const char* cA = S.a_base(cur); const char* cB = S.b_base(cur);
;     PG8_STAGE(PG8_SB(0, 0), cB, voffB); PG8_STAGE(PG8_SB(0, 1), cB + hstep, voffB); PG8_STAGE(PG8_SA(0, 0), cA, oA[0]); PG8_STAGE(PG8_SA(0, 1), cA, oA[1]);
;     if (wr == 1) PG8_BAR;
;     PG8_WAIT_V(2); PG8_BAR;
;     PG8_STAGE(PG8_SB(1, 0), cB + kstep, voffB); PG8_STAGE(PG8_SA(1, 0), cA + kstep, oA[0]); PG8_STAGE(PG8_SB(1, 1), cB + hstep + kstep, voffB);
;     PG8_WAIT_V(6); PG8_BAR;
.LBB0_1033:
	v_readlane_b32 s44, v254, 62
	v_readlane_b32 s45, v254, 63
	s_lshl_b64 s[10:11], s[44:45], 12
	s_add_u32 s9, s42, s10
	s_addc_u32 s17, s43, s11
	v_readlane_b32 s10, v254, 60
	v_readlane_b32 s11, v254, 61
	s_and_b64 s[10:11], s[10:11], exec
	s_cselect_b32 s43, s17, 0
	s_cselect_b32 s42, s9, 0
	s_lshl_b64 s[10:11], s[44:45], 11
	s_add_u32 s9, s40, s10
	s_addc_u32 s10, s41, s11
	s_add_u32 s44, s9, 0x7fc0000
	s_addc_u32 s45, s10, 0
	s_lshl_b32 s9, s8, 5
	s_add_i32 s89, s7, 0x18000
	s_and_b32 s88, s9, 0x60
	s_add_i32 s90, s89, s5
	s_lshl_b32 s87, s4, 6
	s_lshl_b32 s4, s4, 13
	s_lshl_b32 s9, s88, 7
	v_lshl_add_u64 v[12:13], v[12:13], 0, s[24:25]
	s_mov_b32 m0, s90
	s_add_i32 s91, s90, 0x2000
	s_add_i32 s92, s6, 0x8000
	s_add_i32 s93, s6, 0xa000
	global_load_lds_dwordx4 v[12:13], off
	v_lshl_add_u64 v[10:11], v[10:11], 0, s[24:25]
	s_mov_b32 m0, s91
	s_add_u32 s10, s60, 0x20080
	global_load_lds_dwordx4 v[10:11], off
	v_lshl_add_u64 v[6:7], v[6:7], 0, s[24:25]
	s_mov_b32 m0, s92
	s_addc_u32 s11, s61, 0
	s_add_i32 s94, s7, 0x1c000
	global_load_lds_dwordx4 v[6:7], off
	v_lshl_add_u64 v[6:7], v[8:9], 0, s[24:25]
	s_mov_b32 m0, s93
	s_add_i32 s95, s94, s5
	global_load_lds_dwordx4 v[6:7], off
	v_lshl_add_u64 v[6:7], s[10:11], 0, v[2:3]
	s_mov_b32 m0, s95
	s_add_i32 s96, s95, 0x2000
	global_load_lds_dwordx4 v[6:7], off
	v_lshl_add_u64 v[6:7], s[10:11], 0, v[166:167]
	s_mov_b32 m0, s96
	v_bfe_u32 v5, v14, 4, 2
	global_load_lds_dwordx4 v[6:7], off
	v_and_b32_e32 v1, 15, v14
	v_lshlrev_b32_e32 v6, 4, v5
	v_lshlrev_b32_e32 v7, 2, v14
	v_lshl_or_b32 v6, v1, 6, v6
	v_and_b32_e32 v7, 32, v7
	v_bitop3_b32 v8, v6, s4, v7 bitop3:0xde
	v_bitop3_b32 v188, v6, s9, v7 bitop3:0xde
	v_lshlrev_b32_e32 v6, 12, v19
	v_and_b32_e32 v6, 0x7fffe000, v6
	v_lshl_add_u32 v6, v20, 9, v6
	v_or_b32_e32 v6, v6, v21
	v_add_u32_sdwa v6, v6, sext(v22) dst_sel:DWORD dst_unused:UNUSED_PAD src0_sel:DWORD src1_sel:WORD_0
	v_mov_b32_e32 v9, 0x20000
	v_lshl_add_u32 v6, v6, 1, v9
	v_mov_b32_e32 v7, v4
	v_lshl_add_u64 v[176:177], v[6:7], 0, s[26:27]
	v_lshlrev_b32_e32 v6, 12, v15
	v_and_b32_e32 v6, 0x7fffe000, v6
	v_lshl_add_u32 v6, v16, 9, v6
	v_or_b32_e32 v6, v6, v17
	s_waitcnt vmcnt(8)
	s_barrier
	s_waitcnt vmcnt(6)
	s_cmp_lt_u32 s8, 4
	v_add_u32_sdwa v6, v6, sext(v18) dst_sel:DWORD dst_unused:UNUSED_PAD src0_sel:DWORD src1_sel:WORD_0
	s_sext_i32_i8 s5, s46
	s_cselect_b64 s[46:47], -1, 0
	s_cmp_lg_u64 s[42:43], 0
	v_lshl_add_u32 v6, v6, 1, v9
	v_mov_b32_e32 v171, v4
	v_mov_b32_e32 v175, v4
	s_mov_b32 s97, 0
	s_cselect_b64 s[48:49], -1, 0
	s_ashr_i32 s4, s38, 31
	v_lshl_add_u64 v[178:179], v[6:7], 0, s[26:27]
	v_add_u32_e32 v189, s7, v8
	s_barrier
	s_branch .LBB0_1036

; #define PG8_STAGE(bufoff, gbase, voff) do { _Pragma("unroll") for (int _i = 0; _i < 2; ++_i) \
;         __builtin_amdgcn_global_load_lds((const unsigned*)((const char*)(gbase) + (voff)[_i]), (LAS unsigned*)(lds + (bufoff) + ldsw + _i * 8192), 16, 0, 0); } while (0)
; #define PG8_WAIT_V(n) asm volatile("s_waitcnt vmcnt(" #n ")" ::: "memory")
; #define PG8_BAR __builtin_amdgcn_s_barrier()
; template <class Epi, class Sched, bool F8 = false>
; DI void gemm_phase(LAS unsigned char* lds, const int K, const Sched& S, const Epi& E) {
;     ...
;     unsigned oA[2][2]; S.a_off(cur, tid, oA);
;     const char* cA = S.a_base(cur); const char* cB = S.b_base(cur);
;     PG8_STAGE(PG8_SB(0, 0), cB, voffB); PG8_STAGE(PG8_SB(0, 1), cB + hstep, voffB); PG8_STAGE(PG8_SA(0, 0), cA, oA[0]); PG8_STAGE(PG8_SA(0, 1), cA, oA[1]);
;     if (wr == 1) PG8_BAR;
;     PG8_WAIT_V(2); PG8_BAR;
;     PG8_STAGE(PG8_SB(1, 0), cB + kstep, voffB); PG8_STAGE(PG8_SA(1, 0), cA + kstep, oA[0]); PG8_STAGE(PG8_SB(1, 1), cB + hstep + kstep, voffB);
;     PG8_WAIT_V(6); PG8_BAR;
.LBB0_1354:
	v_bfe_u32 v238, v10, 4, 2
	s_add_u32 s46, s62, 0x20bc0000
	v_and_b32_e32 v237, 15, v10
	v_lshlrev_b32_e32 v11, 4, v238
	v_lshlrev_b32_e32 v10, 2, v10
	s_addc_u32 s47, s63, 0
	s_lshl_b32 s68, s8, 6
	v_lshl_or_b32 v11, v237, 6, v11
	s_lshl_b32 s8, s8, 13
	v_and_b32_e32 v10, 32, v10
	v_bitop3_b32 v12, v11, s8, v10 bitop3:0xde
	s_lshl_b32 s8, s6, 5
	s_add_i32 s81, s38, 0x18000
	s_and_b32 s80, s8, 0x60
	s_add_i32 s83, s81, s7
	s_lshl_b32 s8, s80, 7
	s_add_i32 s82, s83, 0x2000
	s_add_u32 s48, s62, 0x3fc0080
	v_lshl_add_u64 v[6:7], v[6:7], 0, s[24:25]
	s_mov_b32 m0, s83
	s_addc_u32 s49, s63, 0
	s_add_i32 s84, s5, 0x8000
	s_add_i32 s85, s5, 0xa000
	v_mov_b32_e32 v215, v4
	v_bitop3_b32 v239, v11, s8, v10 bitop3:0xde
	global_load_lds_dwordx4 v[6:7], off
	v_lshl_add_u64 v[6:7], v[8:9], 0, s[24:25]
	s_mov_b32 m0, s82
	s_add_u32 s8, s60, 0x20080
	v_mov_b32_e32 v219, v4
	global_load_lds_dwordx4 v[6:7], off
	v_lshl_add_u64 v[6:7], s[48:49], 0, v[214:215]
	s_mov_b32 m0, s84
	s_addc_u32 s9, s61, 0
	s_add_i32 s86, s38, 0x1c000
	global_load_lds_dwordx4 v[6:7], off
	v_lshl_add_u64 v[6:7], s[48:49], 0, v[218:219]
	s_mov_b32 m0, s85
	s_add_i32 s88, s86, s7
	global_load_lds_dwordx4 v[6:7], off
	v_lshl_add_u64 v[6:7], s[8:9], 0, v[212:213]
	s_mov_b32 m0, s88
	s_add_i32 s87, s88, 0x2000
	global_load_lds_dwordx4 v[6:7], off
	v_lshl_add_u64 v[6:7], s[8:9], 0, v[2:3]
	s_mov_b32 m0, s87
	s_cmp_lt_u32 s6, 4
	global_load_lds_dwordx4 v[6:7], off
	s_cselect_b64 s[16:17], -1, 0
	s_add_u32 s50, s62, 0x3fc0100
	s_waitcnt vmcnt(8)
	s_barrier
	s_waitcnt vmcnt(6)
	s_addc_u32 s51, s63, 0
	s_add_u32 s52, s62, 0x3fc0180
	v_writelane_b32 v254, s62, 55
	s_addc_u32 s53, s63, 0
	s_mov_b32 s89, 0
	v_writelane_b32 v254, s63, 56
	v_add_u32_e32 v240, s38, v12
	s_mov_b32 s2, 0x20000
	s_barrier
	s_branch .LBB0_1357

; #define PG8_STAGE(bufoff, gbase, voff) do { _Pragma("unroll") for (int _i = 0; _i < 2; ++_i) \
;         __builtin_amdgcn_global_load_lds((const unsigned*)((const char*)(gbase) + (voff)[_i]), (LAS unsigned*)(lds + (bufoff) + ldsw + _i * 8192), 16, 0, 0); } while (0)
; #define PG8_WAIT_V(n) asm volatile("s_waitcnt vmcnt(" #n ")" ::: "memory")
; #define PG8_BAR __builtin_amdgcn_s_barrier()
; template <class Epi, class Sched, bool F8 = false>
; DI void gemm_phase(LAS unsigned char* lds, const int K, const Sched& S, const Epi& E) {
;     ...
;     unsigned oA[2][2]; S.a_off(cur, tid, oA);
;     const char* cA = S.a_base(cur); const char* cB = S.b_base(cur);
;     PG8_STAGE(PG8_SB(0, 0), cB, voffB); PG8_STAGE(PG8_SB(0, 1), cB + hstep, voffB); PG8_STAGE(PG8_SA(0, 0), cA, oA[0]); PG8_STAGE(PG8_SA(0, 1), cA, oA[1]);
;     if (wr == 1) PG8_BAR;
;     PG8_WAIT_V(2); PG8_BAR;
;     PG8_STAGE(PG8_SB(1, 0), cB + kstep, voffB); PG8_STAGE(PG8_SA(1, 0), cA + kstep, oA[0]); PG8_STAGE(PG8_SB(1, 1), cB + hstep + kstep, voffB);
;     PG8_WAIT_V(6); PG8_BAR;
.LBB0_1633:
	s_add_u32 s56, s46, 0x313c0000
	s_addc_u32 s57, s47, 0
	s_add_u32 s2, s46, 0xffc0000
	v_bfe_u32 v5, v14, 4, 2
	v_writelane_b32 v254, s2, 38
	v_writelane_b32 v255, s46, 48
	s_addc_u32 s2, s47, 0
	v_and_b32_e32 v1, 15, v14
	v_lshlrev_b32_e32 v19, 4, v5
	v_lshlrev_b32_e32 v14, 2, v14
	v_writelane_b32 v254, s2, 34
	s_lshl_b32 s2, s1, 6
	v_lshl_or_b32 v19, v1, 6, v19
	s_lshl_b32 s1, s1, 13
	v_and_b32_e32 v14, 32, v14
	v_bitop3_b32 v20, v19, s1, v14 bitop3:0xde
	s_lshl_b32 s1, s0, 5
	s_add_i32 s96, s38, 0x18000
	s_and_b32 s95, s1, 0x60
	s_add_i32 s5, s96, s6
	s_lshl_b32 s1, s95, 7
	v_lshl_add_u64 v[10:11], v[10:11], 0, s[24:25]
	s_mov_b32 m0, s5
	s_add_i32 s97, s5, 0x2000
	s_add_i32 s80, s88, 0x8000
	s_add_i32 s81, s88, 0xa000
	global_load_lds_dwordx4 v[10:11], off
	v_lshl_add_u64 v[8:9], v[8:9], 0, s[24:25]
	s_mov_b32 m0, s97
	s_add_u32 s8, s50, 0x20080
	global_load_lds_dwordx4 v[8:9], off
	v_lshl_add_u64 v[6:7], v[6:7], 0, s[24:25]
	s_mov_b32 m0, s80
	s_addc_u32 s9, s51, 0
	s_add_i32 s4, s38, 0x1c000
	global_load_lds_dwordx4 v[6:7], off
	v_lshl_add_u64 v[6:7], v[12:13], 0, s[24:25]
	s_mov_b32 m0, s81
	s_add_i32 s79, s4, s6
	global_load_lds_dwordx4 v[6:7], off
	v_lshl_add_u64 v[6:7], s[8:9], 0, v[2:3]
	s_mov_b32 m0, s79
	s_add_i32 s78, s79, 0x2000
	global_load_lds_dwordx4 v[6:7], off
	v_lshl_add_u64 v[6:7], s[8:9], 0, v[166:167]
	s_mov_b32 m0, s78
	s_cmp_lt_u32 s0, 4
	global_load_lds_dwordx4 v[6:7], off
	v_writelane_b32 v255, s47, 49
	s_cselect_b64 s[58:59], -1, 0
	s_add_i32 s0, s38, 0x27f04
	v_writelane_b32 v255, s0, 36
	s_add_i32 s0, s38, 0x27f08
	v_writelane_b32 v255, s0, 16
	s_add_i32 s0, s38, 0x27f0c
	v_writelane_b32 v255, s0, 20
	s_add_i32 s0, s38, 0x27f10
	v_writelane_b32 v254, s2, 36
	v_writelane_b32 v255, s0, 26
	s_add_i32 s0, s38, 0x27f14
	v_writelane_b32 v254, s0, 40
	s_add_i32 s0, s38, 0x27f18
	v_writelane_b32 v254, s0, 57
	s_add_i32 s0, s38, 0x27f1c
	v_writelane_b32 v255, s0, 18
	s_add_i32 s0, s38, 0x27f20
	v_writelane_b32 v255, s0, 0
	s_add_i32 s0, s38, 0x27f24
	v_writelane_b32 v255, s0, 4
	s_add_i32 s0, s38, 0x27f28
	v_writelane_b32 v255, s0, 8
	s_add_i32 s0, s38, 0x27f2c
	v_writelane_b32 v255, s0, 14
	s_add_i32 s0, s38, 0x27f30
	v_writelane_b32 v255, s0, 28
	s_add_i32 s0, s38, 0x27f34
	v_writelane_b32 v255, s0, 10
	s_add_i32 s0, s38, 0x27f38
	s_waitcnt vmcnt(8)
	s_barrier
	s_waitcnt vmcnt(6)
	v_writelane_b32 v255, s0, 22
	s_add_i32 s0, s38, 0x27f3c
	v_writelane_b32 v255, s0, 24
	s_mov_b32 s0, 0x20000
	v_bitop3_b32 v177, v19, s1, v14 bitop3:0xde
	v_add3_u32 v176, v15, v17, s0
	v_add3_u32 v178, v16, v18, s0
	s_mov_b32 s92, 0
	v_add_u32_e32 v179, s38, v20
	s_mov_b32 s2, s17
	s_barrier
	s_branch .LBB0_1636
